# v43_touch
# speedup vs baseline: 1.0157x; 1.0056x over previous
_Z10k_enc_scanPKDF16_PKfS2_S2_S2_S2_S2_S2_S2_S2_S2_S0_S2_S2_S2_S2_S2_S0_S2_PfPjS2_S2_S2_S2_S2_S2_S2_S2_S2_S2_S2_S2_PDF16_S5_S3_:
	s_load_dwordx4 s[52:55], s[0:1], 0x98
	s_cmp_gt_u32 s2, 15
	s_mov_b64 s[4:5], -1
	s_cbranch_scc0 .LBB3_39
	s_add_i32 s3, s2, -16
	s_cmpk_gt_i32 s3, 0x33f
	s_cbranch_scc1 .LBB3_38
	v_add_u32_e32 v5, 0x140, v0
	v_add_u32_e32 v6, 0x280, v0
	v_mul_u32_u24_e32 v3, 0x5f5, v5
	v_add_u32_e32 v7, 0x3c0, v0
	v_lshrrev_b32_e32 v10, 17, v3
	v_mul_u32_u24_e32 v3, 0xbe9, v6
	v_add_u32_e32 v8, 0x500, v0
	v_lshrrev_b32_e32 v11, 18, v3
	v_mul_u32_u24_e32 v3, 0xbe9, v7
	v_add_u32_e32 v2, 0x640, v0
	v_lshrrev_b32_e32 v12, 18, v3
	v_mul_u32_u24_e32 v3, 0xbe9, v8
	s_load_dwordx2 s[20:21], s[0:1], 0x90
	s_load_dwordx4 s[56:59], s[0:1], 0x80
	s_load_dwordx8 s[12:19], s[0:1], 0x60
	s_load_dwordx8 s[24:31], s[0:1], 0x40
	s_load_dwordx8 s[36:43], s[0:1], 0x0
	s_load_dwordx8 s[44:51], s[0:1], 0x20
	v_lshrrev_b32_e32 v14, 18, v3
	v_mul_u32_u24_e32 v3, 0x17d1, v2
	s_movk_i32 s4, 0xffaa
	v_lshrrev_b32_e32 v16, 19, v3
	v_mad_i32_i24 v116, v16, s4, v2
	v_mul_u32_u24_e32 v2, 22, v0
	v_mov_b32_e32 v67, 0
	v_lshlrev_b32_e32 v66, 2, v2
	v_mul_u32_u24_e32 v2, 11, v0
	s_waitcnt lgkmcnt(0)
	v_lshl_add_u64 v[72:73], s[40:41], 0, v[66:67]
	v_lshlrev_b32_e32 v66, 2, v2
	v_lshrrev_b32_e32 v2, 1, v0
	v_lshl_add_u64 v[76:77], s[44:45], 0, v[66:67]
	v_and_b32_e32 v117, 0xfc, v2
	v_and_b32_e32 v2, 0x1c0, v0
	s_movk_i32 s8, 0xc0
	v_add_u32_e32 v66, 0xffffff40, v0
	v_cmp_eq_u32_e64 s[8:9], s8, v2
	v_lshlrev_b64 v[2:3], 2, v[66:67]
	v_lshl_add_u64 v[88:89], s[14:15], 0, v[2:3]
	v_lshl_add_u64 v[90:91], s[56:57], 0, v[2:3]
	v_lshl_add_u64 v[92:93], s[12:13], 0, v[2:3]
	v_lshl_add_u64 v[94:95], s[18:19], 0, v[2:3]
	v_lshl_add_u64 v[96:97], s[16:17], 0, v[2:3]
	v_mul_u32_u24_e32 v2, 0x5556, v0
	v_mov_b32_e32 v3, -3
	s_movk_i32 s18, 0x1a0
	v_mul_i32_i24_sdwa v3, v2, v3 dst_sel:DWORD dst_unused:UNUSED_PAD src0_sel:WORD_1 src1_sel:DWORD
	v_mul_u32_u24_sdwa v19, v2, s18 dst_sel:DWORD dst_unused:UNUSED_PAD src0_sel:WORD_1 src1_sel:DWORD
	v_mul_u32_u24_e32 v2, 0xa3e, v0
	v_lshrrev_b32_e32 v2, 12, v2
	v_mad_i32_i24 v112, v10, s4, v5
	v_mad_i32_i24 v113, v11, s4, v6
	v_mad_i32_i24 v114, v12, s4, v7
	v_mad_i32_i24 v115, v14, s4, v8
	v_add_lshl_u32 v20, v3, v0, 4
	v_mul_u32_u24_e32 v3, 0xa3e, v5
	v_mul_u32_u24_e32 v5, 0xa3e, v6
	v_mul_u32_u24_e32 v6, 0xa3e, v7
	v_mul_u32_u24_e32 v7, 0xa3e, v8
	v_and_b32_e32 v2, 0x1f0, v2
	v_lshlrev_b32_e32 v8, 4, v0
	v_add_u32_e32 v123, v2, v8
	v_lshrrev_b32_e32 v2, 12, v3
	v_and_b32_e32 v2, 0x3f0, v2
	v_add_u32_e32 v124, v2, v8
	v_lshrrev_b32_e32 v2, 12, v5
	v_and_b32_e32 v2, 0x7f0, v2
	v_add_u32_e32 v125, v2, v8
	v_lshrrev_b32_e32 v2, 12, v6
	v_and_b32_e32 v2, 0x7f0, v2
	v_mul_u32_u24_e32 v1, 0x2fb, v0
	v_add_u32_e32 v126, v2, v8
	v_lshrrev_b32_e32 v2, 12, v7
	v_and_b32_e32 v4, 63, v0
	v_lshrrev_b32_e32 v9, 16, v1
	v_and_b32_e32 v2, 0x7f0, v2
	v_mad_i32_i24 v1, v9, s4, v0
	v_and_b32_e32 v18, 15, v0
	v_add_u32_e32 v127, v2, v8
	v_lshrrev_b32_e32 v2, 2, v0
	s_movk_i32 s19, 0x70
	v_and_b32_e32 v98, 48, v0
	v_lshlrev_b32_e32 v66, 4, v4
	v_mov_b32_e32 v99, v67
	v_mov_b32_e32 v4, 0xfffff920
	v_and_or_b32 v128, v2, s19, v18
	v_lshl_add_u64 v[102:103], s[20:21], 0, v[98:99]
	v_mad_u64_u32 v[2:3], s[20:21], s2, 22, v[0:1]
	v_mov_b32_e32 v5, -1
	v_mad_u64_u32 v[104:105], s[20:21], v2, 5, v[4:5]
	v_min_u32_e32 v13, 21, v12
	v_min_u32_e32 v15, 21, v14
	v_min_u32_e32 v17, 21, v16
	s_movk_i32 s20, 0x410
	v_mov_b32_e32 v2, 0xfffa6a00
	v_mad_u32_u24 v99, v17, s20, v2
	v_mad_u32_u24 v105, v15, s20, v2
	v_mad_u32_u24 v130, v13, s20, v2
	v_mad_u32_u24 v131, v11, s20, v2
	v_mad_u32_u24 v132, v10, s20, v2
	v_mad_u32_u24 v133, v9, s20, v2
	v_lshlrev_b32_e32 v2, 6, v0
	s_mul_i32 s20, s2, 0x42000
	v_and_b32_e32 v2, 0x7000, v2
	v_add_u32_e32 v2, s20, v2
	v_lshlrev_b32_e32 v3, 8, v18
	v_lshlrev_b32_e32 v68, 2, v0
	v_mov_b32_e32 v69, v67
	s_movk_i32 s6, 0xb0
	s_movk_i32 s10, 0x102
	v_mul_lo_u32 v21, v1, s18
	v_lshlrev_b32_e32 v22, 4, v9
	v_mul_lo_u32 v23, v112, s18
	v_lshlrev_b32_e32 v24, 4, v10
	v_mul_lo_u32 v25, v113, s18
	v_lshlrev_b32_e32 v26, 4, v11
	s_movk_i32 s12, 0x3a4
	v_mul_lo_u32 v27, v114, s18
	v_lshlrev_b32_e32 v12, 4, v12
	s_movk_i32 s14, 0x264
	v_mul_lo_u32 v28, v115, s18
	v_lshlrev_b32_e32 v14, 4, v14
	s_movk_i32 s16, 0x124
	v_mul_lo_u32 v29, v116, s18
	v_lshlrev_b32_e32 v16, 4, v16
	v_mul_u32_u24_e32 v6, 0x1a0, v128
	v_or3_b32 v2, v2, v3, v98
	v_lshlrev_b32_e32 v106, 4, v0
	v_cmp_gt_u32_e64 s[22:23], 22, v0
	v_cmp_gt_u32_e64 s[4:5], 11, v0
	v_lshl_add_u64 v[70:71], s[42:43], 0, v[68:69]
	v_lshl_add_u64 v[74:75], s[46:47], 0, v[68:69]
	v_cmp_gt_u32_e64 s[6:7], s6, v0
	v_lshl_add_u64 v[78:79], s[50:51], 0, v[68:69]
	v_lshl_add_u64 v[80:81], s[28:29], 0, v[68:69]
	v_lshl_add_u64 v[82:83], s[48:49], 0, v[68:69]
	v_lshl_add_u64 v[84:85], s[26:27], 0, v[68:69]
	v_lshl_add_u64 v[86:87], s[24:25], 0, v[68:69]
	v_cmp_gt_u32_e64 s[10:11], s10, v0
	v_lshlrev_b32_e32 v69, 5, v9
	v_lshlrev_b32_e32 v118, 5, v10
	v_lshlrev_b32_e32 v119, 5, v11
	v_cmp_gt_u32_e64 s[12:13], s12, v0
	v_lshlrev_b32_e32 v120, 5, v13
	v_cmp_gt_u32_e64 s[14:15], s14, v0
	v_lshlrev_b32_e32 v121, 5, v15
	v_cmp_gt_u32_e64 s[16:17], s16, v0
	v_lshlrev_b32_e32 v122, 5, v17
	v_mad_u32_u24 v129, v18, s18, v98
	s_mov_b32 s27, 0x20000
	s_mov_b32 s26, 0x1080000
	s_and_b32 s25, s53, 0xffff
	s_mov_b32 s24, s52
	v_lshl_add_u64 v[100:101], s[58:59], 0, v[66:67]
	v_cmp_eq_u32_e64 s[18:19], 0, v0
	s_mul_i32 s29, s2, 0x5960
	s_movk_i32 s33, 0x7000
	v_add_u32_e32 v134, 0xffbe0000, v2
	v_mov_b32_e32 v108, v106
	v_mov_b32_e32 v109, v67
	s_movk_i32 s35, 0x1000
	s_movk_i32 s41, 0x2000
	s_movk_i32 s43, 0x3000
	s_movk_i32 s45, 0x5000
	s_movk_i32 s47, 0x6000
	s_mov_b32 s49, 0x8000
	s_mov_b32 s60, 0xa000
	s_mov_b32 s61, 0xb000
	s_mov_b32 s28, 0x3f3504f3
	s_mov_b32 s62, 0x378e98ab
	s_mov_b32 s63, 0x3b7cd369
	s_mov_b32 s64, 0xbcc618b2
	s_mov_b32 s65, 0x3dda74e4
	s_mov_b32 s66, 0x3f228afd
	s_mov_b32 s67, 0x3e03c728
	s_mov_b32 s68, 0xbfb8aa3b
	s_mov_b32 s69, 0x42ce8ed0
	s_mov_b32 s70, 0xc2b17218
	v_mov_b32_e32 v135, 0x3ba10414
	s_brev_b32 s71, -2
	s_mov_b32 s72, 0xf800000
	v_mov_b32_e32 v136, 0x260
	v_add_u32_e32 v137, v19, v20
	s_movk_i32 s73, 0x401
	s_mov_b32 s74, 0x3ea7ba05
	s_mov_b32 s34, 0xbfba00e3
	s_mov_b32 s40, 0x3f87dc22
	s_mov_b32 s42, 0x3fb5f0e3
	v_add_u32_e32 v138, v21, v22
	v_add_u32_e32 v139, v23, v24
	v_add_u32_e32 v140, v25, v26
	v_add_u32_e32 v141, v27, v12
	v_add_u32_e32 v142, v28, v14
	v_add_u32_e32 v143, v29, v16
	v_add_u32_e32 v144, v98, v6
	s_mov_b32 s75, 0x12000
	s_mov_b32 s76, 0x14000
	s_mov_b32 s77, 0x15000
	s_mov_b32 s78, 0x16000
	s_mov_b32 s79, 0x17000
	s_mov_b32 s80, 0x19000
	s_mov_b32 s81, 0x1a000
	s_mov_b32 s82, 0x1b000
	s_mov_b32 s83, 0x1c000
	s_mov_b32 s84, 0x1e000
	s_mov_b32 s85, 0x1f000
	s_mov_b32 s86, 0x21000
	s_mov_b32 s87, 0x23000
	s_mov_b32 s88, 0x24000
	s_mov_b32 s89, 0x25000
	s_mov_b32 s90, 0x26000
	s_mov_b32 s91, 0x28000
	s_mov_b32 s92, 0x29000
	s_mov_b32 s93, 0x2a000
	v_mov_b32_e32 v145, 1
	v_mov_b32_e32 v146, 0xb9c68948
	v_mov_b32_e32 v147, 0x7f800000
	v_mov_b32_e32 v148, v67
	v_mov_b32_e32 v149, v67
	v_mov_b32_e32 v150, v67
	v_mov_b32_e32 v151, v67
	s_mov_b32 s44, 0xbe91a98e
	s_mov_b32 s46, 0x3e827906
	s_mov_b32 s48, 0x4038aa3b
	s_mov_b64 s[98:99], exec
	s_and_b64 exec, s[98:99], s[4:5]
	global_load_dword v244, v[70:71], off
	global_load_dword v245, v[72:73], off
	global_load_dword v246, v[72:73], off offset:64
	s_and_b64 exec, s[98:99], s[22:23]
	global_load_dword v247, v[76:77], off
	global_load_dword v248, v[74:75], off
	s_and_b64 exec, s[98:99], s[6:7]
	global_load_dword v249, v[80:81], off
	global_load_dword v250, v[78:79], off
	global_load_dword v251, v[82:83], off
	global_load_dword v252, v[84:85], off
	global_load_dword v253, v[86:87], off
	s_mov_b64 exec, s[98:99]
	s_branch .LBB3_4

	.amdhsa_kernel _Z10k_enc_scanPKDF16_PKfS2_S2_S2_S2_S2_S2_S2_S2_S2_S0_S2_S2_S2_S2_S2_S0_S2_PfPjS2_S2_S2_S2_S2_S2_S2_S2_S2_S2_S2_S2_PDF16_S5_S3_
		.amdhsa_group_segment_fixed_size 91136
		.amdhsa_private_segment_fixed_size 0
		.amdhsa_kernarg_size 288
		.amdhsa_user_sgpr_count 2
		.amdhsa_user_sgpr_dispatch_ptr 0
		.amdhsa_user_sgpr_queue_ptr 0
		.amdhsa_user_sgpr_kernarg_segment_ptr 1
		.amdhsa_user_sgpr_dispatch_id 0
		.amdhsa_user_sgpr_kernarg_preload_length 0
		.amdhsa_user_sgpr_kernarg_preload_offset 0
		.amdhsa_user_sgpr_private_segment_size 0
		.amdhsa_uses_dynamic_stack 0
		.amdhsa_enable_private_segment 0
		.amdhsa_system_sgpr_workgroup_id_x 1
		.amdhsa_system_sgpr_workgroup_id_y 0
		.amdhsa_system_sgpr_workgroup_id_z 0
		.amdhsa_system_sgpr_workgroup_info 0
		.amdhsa_system_vgpr_workitem_id 0
		.amdhsa_next_free_vgpr 254
		.amdhsa_next_free_sgpr 100
		.amdhsa_accum_offset 256
		.amdhsa_reserve_vcc 1
		.amdhsa_float_round_mode_32 0
		.amdhsa_float_round_mode_16_64 0
		.amdhsa_float_denorm_mode_32 3
		.amdhsa_float_denorm_mode_16_64 3
		.amdhsa_dx10_clamp 1
		.amdhsa_ieee_mode 1
		.amdhsa_fp16_overflow 0
		.amdhsa_tg_split 0
		.amdhsa_exception_fp_ieee_invalid_op 0
		.amdhsa_exception_fp_denorm_src 0
		.amdhsa_exception_fp_ieee_div_zero 0
		.amdhsa_exception_fp_ieee_overflow 0
		.amdhsa_exception_fp_ieee_underflow 0
		.amdhsa_exception_fp_ieee_inexact 0
		.amdhsa_exception_int_div_zero 0
	.end_amdhsa_kernel

amdhsa.kernels:
  - .agpr_count:     8
    .args:
      - .actual_access:  read_only
        .address_space:  global
        .offset:         0
        .size:           8
        .value_kind:     global_buffer
      - .actual_access:  read_only
        .address_space:  global
        .offset:         8
        .size:           8
        .value_kind:     global_buffer
      - .actual_access:  write_only
        .address_space:  global
        .offset:         16
        .size:           8
        .value_kind:     global_buffer
      - .actual_access:  write_only
        .address_space:  global
        .offset:         24
        .size:           8
        .value_kind:     global_buffer
      - .actual_access:  read_only
        .address_space:  global
        .offset:         32
        .size:           8
        .value_kind:     global_buffer
      - .actual_access:  read_only
        .address_space:  global
        .offset:         40
        .size:           8
        .value_kind:     global_buffer
      - .actual_access:  write_only
        .address_space:  global
        .offset:         48
        .size:           8
        .value_kind:     global_buffer
      - .actual_access:  write_only
        .address_space:  global
        .offset:         56
        .size:           8
        .value_kind:     global_buffer
      - .actual_access:  write_only
        .address_space:  global
        .offset:         64
        .size:           8
        .value_kind:     global_buffer
    .group_segment_fixed_size: 24976
    .kernarg_segment_align: 8
    .kernarg_segment_size: 72
    .language:       OpenCL C
    .language_version:
      - 2
      - 0
    .max_flat_workgroup_size: 256
    .name:           _Z9k_fb_mfmaPKfS0_PDF16_PfS0_S0_S1_S1_Pj
    .private_segment_fixed_size: 0
    .sgpr_count:     24
    .sgpr_spill_count: 0
    .symbol:         _Z9k_fb_mfmaPKfS0_PDF16_PfS0_S0_S1_S1_Pj.kd
    .uniform_work_group_size: 1
    .uses_dynamic_stack: false
    .vgpr_count:     92
    .vgpr_spill_count: 0
    .wavefront_size: 64
  - .agpr_count:     0
    .args:
      - .actual_access:  read_only
        .address_space:  global
        .offset:         0
        .size:           8
        .value_kind:     global_buffer
      - .actual_access:  read_only
        .address_space:  global
        .offset:         8
        .size:           8
        .value_kind:     global_buffer
      - .actual_access:  write_only
        .address_space:  global
        .offset:         16
        .size:           8
        .value_kind:     global_buffer
      - .actual_access:  write_only
        .address_space:  global
        .offset:         24
        .size:           8
        .value_kind:     global_buffer
    .group_segment_fixed_size: 0
    .kernarg_segment_align: 8
    .kernarg_segment_size: 32
    .language:       OpenCL C
    .language_version:
      - 2
      - 0
    .max_flat_workgroup_size: 1024
    .name:           _Z6k_prepPKfS0_PDF16_S1_
    .private_segment_fixed_size: 0
    .sgpr_count:     19
    .sgpr_spill_count: 0
    .symbol:         _Z6k_prepPKfS0_PDF16_S1_.kd
    .uniform_work_group_size: 1
    .uses_dynamic_stack: false
    .vgpr_count:     8
    .vgpr_spill_count: 0
    .wavefront_size: 64
  - .agpr_count:     0
    .args:
      - .actual_access:  read_only
        .address_space:  global
        .offset:         0
        .size:           8
        .value_kind:     global_buffer
      - .actual_access:  read_only
        .address_space:  global
        .offset:         8
        .size:           8
        .value_kind:     global_buffer
      - .actual_access:  read_only
        .address_space:  global
        .offset:         16
        .size:           8
        .value_kind:     global_buffer
      - .actual_access:  read_only
        .address_space:  global
        .offset:         24
        .size:           8
        .value_kind:     global_buffer
      - .actual_access:  read_only
        .address_space:  global
        .offset:         32
        .size:           8
        .value_kind:     global_buffer
      - .actual_access:  read_only
        .address_space:  global
        .offset:         40
        .size:           8
        .value_kind:     global_buffer
      - .actual_access:  read_only
        .address_space:  global
        .offset:         48
        .size:           8
        .value_kind:     global_buffer
      - .actual_access:  read_only
        .address_space:  global
        .offset:         56
        .size:           8
        .value_kind:     global_buffer
      - .actual_access:  read_only
        .address_space:  global
        .offset:         64
        .size:           8
        .value_kind:     global_buffer
      - .actual_access:  read_only
        .address_space:  global
        .offset:         72
        .size:           8
        .value_kind:     global_buffer
      - .actual_access:  write_only
        .address_space:  global
        .offset:         80
        .size:           8
        .value_kind:     global_buffer
      - .actual_access:  write_only
        .address_space:  global
        .offset:         88
        .size:           8
        .value_kind:     global_buffer
    .group_segment_fixed_size: 236
    .kernarg_segment_align: 8
    .kernarg_segment_size: 96
    .language:       OpenCL C
    .language_version:
      - 2
      - 0
    .max_flat_workgroup_size: 192
    .name:           _Z6k_gatePKfS0_S0_S0_S0_S0_S0_S0_S0_S0_PfPj
    .private_segment_fixed_size: 0
    .sgpr_count:     32
    .sgpr_spill_count: 0
    .symbol:         _Z6k_gatePKfS0_S0_S0_S0_S0_S0_S0_S0_S0_PfPj.kd
    .uniform_work_group_size: 1
    .uses_dynamic_stack: false
    .vgpr_count:     47
    .vgpr_spill_count: 0
    .wavefront_size: 64
  - .agpr_count:     0
    .args:
      - .actual_access:  read_only
        .address_space:  global
        .offset:         0
        .size:           8
        .value_kind:     global_buffer
      - .actual_access:  read_only
        .address_space:  global
        .offset:         8
        .size:           8
        .value_kind:     global_buffer
      - .actual_access:  read_only
        .address_space:  global
        .offset:         16
        .size:           8
        .value_kind:     global_buffer
      - .actual_access:  read_only
        .address_space:  global
        .offset:         24
        .size:           8
        .value_kind:     global_buffer
      - .actual_access:  read_only
        .address_space:  global
        .offset:         32
        .size:           8
        .value_kind:     global_buffer
      - .actual_access:  read_only
        .address_space:  global
        .offset:         40
        .size:           8
        .value_kind:     global_buffer
      - .actual_access:  read_only
        .address_space:  global
        .offset:         48
        .size:           8
        .value_kind:     global_buffer
      - .actual_access:  read_only
        .address_space:  global
        .offset:         56
        .size:           8
        .value_kind:     global_buffer
      - .actual_access:  read_only
        .address_space:  global
        .offset:         64
        .size:           8
        .value_kind:     global_buffer
      - .actual_access:  read_only
        .address_space:  global
        .offset:         72
        .size:           8
        .value_kind:     global_buffer
      - .actual_access:  read_only
        .address_space:  global
        .offset:         80
        .size:           8
        .value_kind:     global_buffer
      - .actual_access:  read_only
        .address_space:  global
        .offset:         88
        .size:           8
        .value_kind:     global_buffer
      - .actual_access:  read_only
        .address_space:  global
        .offset:         96
        .size:           8
        .value_kind:     global_buffer
      - .actual_access:  read_only
        .address_space:  global
        .offset:         104
        .size:           8
        .value_kind:     global_buffer
      - .actual_access:  read_only
        .address_space:  global
        .offset:         112
        .size:           8
        .value_kind:     global_buffer
      - .actual_access:  read_only
        .address_space:  global
        .offset:         120
        .size:           8
        .value_kind:     global_buffer
      - .actual_access:  read_only
        .address_space:  global
        .offset:         128
        .size:           8
        .value_kind:     global_buffer
      - .actual_access:  read_only
        .address_space:  global
        .offset:         136
        .size:           8
        .value_kind:     global_buffer
      - .actual_access:  read_only
        .address_space:  global
        .offset:         144
        .size:           8
        .value_kind:     global_buffer
      - .address_space:  global
        .offset:         152
        .size:           8
        .value_kind:     global_buffer
      - .address_space:  global
        .offset:         160
        .size:           8
        .value_kind:     global_buffer
      - .actual_access:  read_only
        .address_space:  global
        .offset:         168
        .size:           8
        .value_kind:     global_buffer
      - .actual_access:  read_only
        .address_space:  global
        .offset:         176
        .size:           8
        .value_kind:     global_buffer
      - .actual_access:  read_only
        .address_space:  global
        .offset:         184
        .size:           8
        .value_kind:     global_buffer
      - .actual_access:  read_only
        .address_space:  global
        .offset:         192
        .size:           8
        .value_kind:     global_buffer
      - .actual_access:  read_only
        .address_space:  global
        .offset:         200
        .size:           8
        .value_kind:     global_buffer
      - .actual_access:  read_only
        .address_space:  global
        .offset:         208
        .size:           8
        .value_kind:     global_buffer
      - .actual_access:  read_only
        .address_space:  global
        .offset:         216
        .size:           8
        .value_kind:     global_buffer
      - .actual_access:  read_only
        .address_space:  global
        .offset:         224
        .size:           8
        .value_kind:     global_buffer
      - .actual_access:  read_only
        .address_space:  global
        .offset:         232
        .size:           8
        .value_kind:     global_buffer
      - .actual_access:  read_only
        .address_space:  global
        .offset:         240
        .size:           8
        .value_kind:     global_buffer
      - .actual_access:  read_only
        .address_space:  global
        .offset:         248
        .size:           8
        .value_kind:     global_buffer
      - .actual_access:  read_only
        .address_space:  global
        .offset:         256
        .size:           8
        .value_kind:     global_buffer
      - .actual_access:  write_only
        .address_space:  global
        .offset:         264
        .size:           8
        .value_kind:     global_buffer
      - .actual_access:  write_only
        .address_space:  global
        .offset:         272
        .size:           8
        .value_kind:     global_buffer
      - .actual_access:  write_only
        .address_space:  global
        .offset:         280
        .size:           8
        .value_kind:     global_buffer
    .group_segment_fixed_size: 91136
    .kernarg_segment_align: 8
    .kernarg_segment_size: 288
    .language:       OpenCL C
    .language_version:
      - 2
      - 0
    .max_flat_workgroup_size: 320
    .name:           _Z10k_enc_scanPKDF16_PKfS2_S2_S2_S2_S2_S2_S2_S2_S2_S0_S2_S2_S2_S2_S2_S0_S2_PfPjS2_S2_S2_S2_S2_S2_S2_S2_S2_S2_S2_S2_PDF16_S5_S3_
    .private_segment_fixed_size: 0
    .sgpr_count:     106
    .sgpr_spill_count: 0
    .symbol:         _Z10k_enc_scanPKDF16_PKfS2_S2_S2_S2_S2_S2_S2_S2_S2_S0_S2_S2_S2_S2_S2_S0_S2_PfPjS2_S2_S2_S2_S2_S2_S2_S2_S2_S2_S2_S2_PDF16_S5_S3_.kd
    .uniform_work_group_size: 1
    .uses_dynamic_stack: false
    .vgpr_count:     254
    .vgpr_spill_count: 0
    .wavefront_size: 64
  - .agpr_count:     0
    .args:
      - .actual_access:  read_only
        .address_space:  global
        .offset:         0
        .size:           8
        .value_kind:     global_buffer
      - .actual_access:  read_only
        .address_space:  global
        .offset:         8
        .size:           8
        .value_kind:     global_buffer
      - .actual_access:  write_only
        .address_space:  global
        .offset:         16
        .size:           8
        .value_kind:     global_buffer
    .group_segment_fixed_size: 66580
    .kernarg_segment_align: 8
    .kernarg_segment_size: 24
    .language:       OpenCL C
    .language_version:
      - 2
      - 0
    .max_flat_workgroup_size: 320
    .name:           _Z7k_att1nPKDF16_S0_Pf
    .private_segment_fixed_size: 0
    .sgpr_count:     29
    .sgpr_spill_count: 0
    .symbol:         _Z7k_att1nPKDF16_S0_Pf.kd
    .uniform_work_group_size: 1
    .uses_dynamic_stack: false
    .vgpr_count:     126
    .vgpr_spill_count: 0
    .wavefront_size: 64
  - .agpr_count:     0
    .args:
      - .actual_access:  read_only
        .address_space:  global
        .offset:         0
        .size:           8
        .value_kind:     global_buffer
      - .actual_access:  read_only
        .address_space:  global
        .offset:         8
        .size:           8
        .value_kind:     global_buffer
      - .actual_access:  read_only
        .address_space:  global
        .offset:         16
        .size:           8
        .value_kind:     global_buffer
      - .actual_access:  write_only
        .address_space:  global
        .offset:         24
        .size:           8
        .value_kind:     global_buffer
      - .actual_access:  read_only
        .address_space:  global
        .offset:         32
        .size:           8
        .value_kind:     global_buffer
      - .actual_access:  read_only
        .address_space:  global
        .offset:         40
        .size:           8
        .value_kind:     global_buffer
      - .actual_access:  read_only
        .address_space:  global
        .offset:         48
        .size:           8
        .value_kind:     global_buffer
      - .actual_access:  read_only
        .address_space:  global
        .offset:         56
        .size:           8
        .value_kind:     global_buffer
      - .actual_access:  read_only
        .address_space:  global
        .offset:         64
        .size:           8
        .value_kind:     global_buffer
      - .actual_access:  read_only
        .address_space:  global
        .offset:         72
        .size:           8
        .value_kind:     global_buffer
      - .actual_access:  read_only
        .address_space:  global
        .offset:         80
        .size:           8
        .value_kind:     global_buffer
      - .actual_access:  read_only
        .address_space:  global
        .offset:         88
        .size:           8
        .value_kind:     global_buffer
      - .actual_access:  read_only
        .address_space:  global
        .offset:         96
        .size:           8
        .value_kind:     global_buffer
      - .actual_access:  write_only
        .address_space:  global
        .offset:         104
        .size:           8
        .value_kind:     global_buffer
    .group_segment_fixed_size: 70720
    .kernarg_segment_align: 8
    .kernarg_segment_size: 112
    .language:       OpenCL C
    .language_version:
      - 2
      - 0
    .max_flat_workgroup_size: 320
    .name:           _Z7k_att2nPKDF16_S0_PKfPfS2_S2_S2_S2_S2_S2_S2_S2_S2_S3_
    .private_segment_fixed_size: 0
    .sgpr_count:     58
    .sgpr_spill_count: 0
    .symbol:         _Z7k_att2nPKDF16_S0_PKfPfS2_S2_S2_S2_S2_S2_S2_S2_S2_S3_.kd
    .uniform_work_group_size: 1
    .uses_dynamic_stack: false
    .vgpr_count:     122
    .vgpr_spill_count: 0
    .wavefront_size: 64
  - .agpr_count:     0
    .args:
      - .actual_access:  read_only
        .address_space:  global
        .offset:         0
        .size:           8
        .value_kind:     global_buffer
      - .actual_access:  read_only
        .address_space:  global
        .offset:         8
        .size:           8
        .value_kind:     global_buffer
      - .actual_access:  read_only
        .address_space:  global
        .offset:         16
        .size:           8
        .value_kind:     global_buffer
      - .actual_access:  read_only
        .address_space:  global
        .offset:         24
        .size:           8
        .value_kind:     global_buffer
      - .actual_access:  read_only
        .address_space:  global
        .offset:         32
        .size:           8
        .value_kind:     global_buffer
      - .actual_access:  read_only
        .address_space:  global
        .offset:         40
        .size:           8
        .value_kind:     global_buffer
      - .actual_access:  read_only
        .address_space:  global
        .offset:         48
        .size:           8
        .value_kind:     global_buffer
      - .actual_access:  read_only
        .address_space:  global
        .offset:         56
        .size:           8
        .value_kind:     global_buffer
      - .actual_access:  read_only
        .address_space:  global
        .offset:         64
        .size:           8
        .value_kind:     global_buffer
      - .actual_access:  write_only
        .address_space:  global
        .offset:         72
        .size:           8
        .value_kind:     global_buffer
    .group_segment_fixed_size: 704
    .kernarg_segment_align: 8
    .kernarg_segment_size: 80
    .language:       OpenCL C
    .language_version:
      - 2
      - 0
    .max_flat_workgroup_size: 64
    .name:           _Z8k_heads3PKfS0_S0_S0_S0_S0_S0_S0_S0_Pf
    .private_segment_fixed_size: 0
    .sgpr_count:     24
    .sgpr_spill_count: 0
    .symbol:         _Z8k_heads3PKfS0_S0_S0_S0_S0_S0_S0_S0_Pf.kd
    .uniform_work_group_size: 1
    .uses_dynamic_stack: false
    .vgpr_count:     121
    .vgpr_spill_count: 0
    .wavefront_size: 64
